# speedup vs baseline: 1.0075x; 1.0075x over previous
_Z11attn_kernelPKfS0_S0_PKcS2_PKDv4_jS0_S0_S0_S0_Pf:
	s_load_dwordx8 s[4:11], s[0:1], 0x0
	s_load_dwordx8 s[12:19], s[0:1], 0x20
	v_readfirstlane_b32 s20, v0
	s_bfe_u32 s28, s2, 0x10002
	s_lshr_b32 s29, s20, 6
	s_lshr_b32 s3, s20, 8
	s_bfe_u32 s30, s20, 0x20006
	s_lshr_b32 s31, s2, 3
	s_lshl_b32 s24, s28, 18
	s_waitcnt lgkmcnt(0)
	s_add_u32 s20, s10, s24
	s_addc_u32 s10, s11, 0
	s_and_b32 s21, s10, 0xffff
	s_add_u32 s24, s12, s24
	s_addc_u32 s10, s13, 0
	v_and_b32_e32 v1, 63, v0
	s_and_b32 s25, s10, 0xffff
	s_lshl_b32 s10, s30, 10
	s_lshl_b32 s38, s3, 12
	v_lshlrev_b32_e32 v2, 4, v1
	s_or_b32 s35, s10, s38
	v_lshl_or_b32 v2, s3, 17, v2
	s_cmp_lg_u32 0, -1
	v_or_b32_e32 v174, s10, v2
	s_cselect_b32 s10, 0, 0
	s_mov_b32 s36, 0
	s_mov_b32 s23, 0x20000
	s_mov_b32 s22, 0x40000
	s_add_i32 s33, s35, s10
	s_mov_b32 m0, s33
	s_nop 0
	buffer_load_dwordx4 v174, s[20:23], s36 offen lds
	s_mov_b32 s26, s22
	s_mov_b32 s27, s23
	s_add_i32 s34, s33, 0xc000
	s_mov_b32 m0, s34
	s_nop 0
	buffer_load_dwordx4 v174, s[24:27], s36 offen lds
	s_add_i32 s10, s33, 0x4000
	s_movk_i32 s37, 0x1000
	s_mov_b32 m0, s10
	s_nop 0
	buffer_load_dwordx4 v174, s[20:23], s37 offen lds
	s_add_i32 s10, s33, 0x8000
	s_movk_i32 s11, 0x2000
	s_mov_b32 m0, s10
	s_nop 0
	buffer_load_dwordx4 v174, s[20:23], s11 offen lds
	s_lshl_b32 s10, s2, 7
	s_and_b32 s10, s10, 0x380
	s_lshl_b32 s11, s31, 2
	s_add_i32 s10, s10, s11
	s_or_b32 s10, s30, s10
	v_and_b32_e32 v172, 31, v0
	v_lshl_or_b32 v140, s10, 7, v1
	v_mov_b32_e32 v141, 0
	v_lshl_add_u64 v[6:7], v[140:141], 4, s[14:15]
	v_ashrrev_i32_e32 v9, 31, v140
	v_mov_b32_e32 v8, v140
	v_lshl_or_b32 v140, s10, 5, v172
	v_lshlrev_b64 v[4:5], 2, v[140:141]
	v_lshl_add_u64 v[2:3], s[16:17], 0, v[4:5]
	global_load_dword v2, v[2:3], off
	v_lshl_add_u64 v[8:9], v[8:9], 4, s[14:15]
	global_load_dwordx4 v[116:119], v[6:7], off
	global_load_dwordx4 v[120:123], v[8:9], off offset:1024
	s_load_dwordx4 s[12:15], s[0:1], 0x40
	s_load_dwordx2 s[10:11], s[0:1], 0x50
	v_lshlrev_b32_e32 v173, 2, v1
	v_lshl_or_b32 v3, s28, 11, v173
	s_waitcnt lgkmcnt(0)
	global_load_dword v44, v3, s[14:15] offset:256
	global_load_dword v45, v3, s[14:15]
	v_bfe_u32 v175, v0, 5, 1
	v_lshlrev_b32_e32 v0, 11, v175
	v_lshlrev_b32_e32 v3, 4, v172
	s_add_i32 s0, s38, 0
	v_lshl_add_u64 v[4:5], s[12:13], 0, v[4:5]
	v_add3_u32 v176, s0, v0, v3
	global_load_dword v0, v[4:5], off
	v_lshrrev_b32_e32 v124, 2, v1
	v_lshrrev_b32_e32 v125, 4, v1
	v_xor_b32_e32 v124, v124, v125
	v_and_b32_e32 v124, 1, v124
	v_add_u32_e32 v124, -1, v124
	v_and_b32_e32 v124, 0x38383838, v124
	v_mov_b32_e32 v200, 0
	v_mov_b32_e32 v201, 0
	v_mov_b32_e32 v202, 0
	v_mov_b32_e32 v203, 0
	v_mov_b32_e32 v204, 0
	v_mov_b32_e32 v125, v124
	v_mov_b32_e32 v126, v124
	v_mov_b32_e32 v127, v124
	v_mov_b32_e32 v128, v124
	v_mov_b32_e32 v129, v124
	v_mov_b32_e32 v130, v124
	v_mov_b32_e32 v131, v124
	v_mov_b32_e32 v140, 0x7f7f7f7f
	s_mov_b32 s0, 0xf800000
	s_movk_i32 s15, 0x3000
	s_mov_b32 s12, 1
	s_movk_i32 s14, 0x4000
	s_mov_b32 s13, 0x8000
	v_mov_b32_e32 v132, v141
	v_mov_b32_e32 v133, v141
	v_mov_b32_e32 v134, v141
	v_mov_b32_e32 v135, v141
	v_mov_b32_e32 v136, v141
	v_mov_b32_e32 v137, v141
	v_mov_b32_e32 v138, v141
	v_mov_b32_e32 v139, v141
	s_waitcnt vmcnt(5)
	v_mov_b32_e32 v4, v2
	v_mov_b32_e32 v5, v2
	v_mov_b32_e32 v6, v2
	v_mov_b32_e32 v7, v2
	v_mov_b32_e32 v8, v2
	v_mov_b32_e32 v9, v2
	v_mov_b32_e32 v10, v2
	v_mov_b32_e32 v11, v2
	v_mov_b32_e32 v12, v2
	v_mov_b32_e32 v13, v2
	v_mov_b32_e32 v14, v2
	v_mov_b32_e32 v15, v2
	v_mov_b32_e32 v16, v2
	v_mov_b32_e32 v17, v2
	v_mov_b32_e32 v3, v2
	v_mov_b64_e32 v[18:19], v[16:17]
	v_mov_b64_e32 v[16:17], v[14:15]
	v_mov_b64_e32 v[14:15], v[12:13]
	v_mov_b64_e32 v[12:13], v[10:11]
	v_mov_b64_e32 v[10:11], v[8:9]
	v_mov_b64_e32 v[8:9], v[6:7]
	v_mov_b64_e32 v[6:7], v[4:5]
	v_mov_b64_e32 v[4:5], v[2:3]
	s_waitcnt vmcnt(0) lgkmcnt(0)
	s_barrier
	ds_read_b128 v[24:27], v176 offset:1024
	ds_read_b128 v[20:23], v176
	ds_read_b128 v[36:39], v176 offset:512
	ds_read_b128 v[40:43], v176 offset:1536
	ds_read_b128 v[84:87], v176 offset:16384
	ds_read_b128 v[92:95], v176 offset:16896
	ds_read_b128 v[88:91], v176 offset:17408
	ds_read_b128 v[96:99], v176 offset:17920
	s_waitcnt vmcnt(3) lgkmcnt(6)
	v_mfma_f32_32x32x64_f8f6f4 v[20:35], v[20:27], v[116:123], v[4:19]
	s_waitcnt vmcnt(2)
	v_max_f32_e32 v3, v44, v44
	s_waitcnt vmcnt(1)
	v_max_f32_e32 v44, v45, v45
	v_max_f32_e32 v44, v44, v3
	s_nop 1
	v_max_f32_dpp v44, v44, v44 quad_perm:[1,0,3,2] row_mask:0xf bank_mask:0xf
	s_nop 1
	v_max_f32_dpp v44, v44, v44 quad_perm:[2,3,0,1] row_mask:0xf bank_mask:0xf
	s_nop 1
	v_max_f32_dpp v44, v44, v44 row_half_mirror row_mask:0xf bank_mask:0xf
	s_nop 1
	v_max_f32_dpp v44, v44, v44 row_mirror row_mask:0xf bank_mask:0xf
	s_nop 1
	v_max_f32_dpp v44, v44, v44 row_bcast:15 row_mask:0xa bank_mask:0xf
	s_nop 1
	v_max_f32_dpp v44, v44, v44 row_bcast:31 row_mask:0xc bank_mask:0xf
	s_nop 1
	v_readlane_b32 s47, v44, 63
	s_waitcnt vmcnt(0) lgkmcnt(0)
	s_barrier
	v_mfma_f32_32x32x64_f8f6f4 v[4:19], v[36:43], v[116:123], v[4:19]
	s_mov_b32 m0, s33
	s_nop 0
	buffer_load_dwordx4 v174, s[20:23], s15 offen lds
	s_add_i32 s15, s34, 0x4000
	s_mov_b32 m0, s15
	s_nop 0
	buffer_load_dwordx4 v174, s[24:27], s37 offen lds
	s_nop 1
	v_max_f32_e32 v3, v21, v21
	v_max_f32_e32 v36, v20, v20
	v_max_f32_e32 v3, v36, v3
	s_nop 7
	v_max3_f32 v37, v22, v23, v5
	v_max3_f32 v36, v37, v26, v27
	v_max3_f32 v3, v3, v4, v6
	v_max3_f32 v3, v3, v7, v24
	v_max3_f32 v36, v36, v10, v11
	v_max3_f32 v3, v3, v25, v8
	v_max3_f32 v36, v36, v30, v31
	v_max3_f32 v3, v3, v9, v28
	v_max3_f32 v36, v36, v14, v15
	v_max3_f32 v3, v3, v29, v12
	v_max3_f32 v36, v36, v34, v35
	v_max3_f32 v3, v3, v13, v32
	v_max3_f32 v36, v36, v18, v19
	v_max3_f32 v3, v3, v33, v16
	v_max3_f32 v3, v3, v17, v36
	v_mov_b32_e32 v36, v3
	s_nop 1
	v_permlane32_swap_b32_e32 v3, v36
	v_max_f32_e32 v36, v36, v36
	v_max_f32_e32 v3, v3, v3
	v_max_f32_e32 v3, v3, v36
	v_sub_f32_e32 v36, 0xc0400000, v3
	v_add_f32_e32 v20, v36, v20
	v_add_f32_e32 v21, v36, v21
	v_add_f32_e32 v22, v36, v22
	v_add_f32_e32 v23, v36, v23
	v_add_f32_e32 v24, v36, v24
	v_add_f32_e32 v25, v36, v25
	v_add_f32_e32 v26, v36, v26
	v_add_f32_e32 v27, v36, v27
	v_add_f32_e32 v28, v36, v28
	v_add_f32_e32 v29, v36, v29
	v_mov_b32_e32 v37, s47
	v_mul_f32_e32 v38, 0x4f800000, v37
	v_cmp_gt_f32_e32 vcc, s0, v37
	v_add_f32_e32 v30, v36, v30
	v_add_f32_e32 v31, v36, v31
	v_cndmask_b32_e32 v37, v37, v38, vcc
	v_sqrt_f32_e32 v38, v37
	v_add_f32_e32 v32, v36, v32
	v_add_f32_e32 v33, v36, v33
	v_add_f32_e32 v34, v36, v34
	v_add_f32_e32 v35, v36, v35
	v_add_f32_e32 v4, v36, v4
	v_add_f32_e32 v5, v36, v5
	v_add_f32_e32 v6, v36, v6
	v_add_f32_e32 v7, v36, v7
	v_add_f32_e32 v8, v36, v8
	v_add_f32_e32 v9, v36, v9
	v_add_f32_e32 v10, v36, v10
	v_add_f32_e32 v11, v36, v11
	v_add_f32_e32 v12, v36, v12
	v_add_f32_e32 v13, v36, v13
	v_add_f32_e32 v14, v36, v14
	v_add_f32_e32 v15, v36, v15
	v_add_f32_e32 v16, v36, v16
	v_add_f32_e32 v17, v36, v17
	v_add_f32_e32 v18, v36, v18
	v_add_f32_e32 v19, v36, v19
	v_add_u32_e32 v36, -1, v38
	v_fma_f32 v39, -v36, v38, v37
	v_cmp_ge_f32_e64 s[0:1], 0, v39
	v_add_u32_e32 v39, 1, v38
	v_exp_f32_e32 v161, v20
	v_cndmask_b32_e64 v36, v38, v36, s[0:1]
	v_fma_f32 v38, -v39, v38, v37
	v_cmp_lt_f32_e64 s[0:1], 0, v38
	v_exp_f32_e32 v100, v4
	v_exp_f32_e32 v163, v21
	v_cndmask_b32_e64 v36, v36, v39, s[0:1]
	v_mul_f32_e32 v38, 0x37800000, v36
	v_cndmask_b32_e32 v36, v36, v38, vcc
	v_mov_b32_e32 v38, 0x260
	v_cmp_class_f32_e32 vcc, v37, v38
	s_mov_b32 s0, 0x42700000
	v_exp_f32_e32 v148, v5
	v_cndmask_b32_e32 v36, v36, v37, vcc
	s_waitcnt vmcnt(0)
	v_mul_f32_e32 v0, v36, v0
	v_mul_f32_e32 v0, 0x3f91eb85, v0
	v_exp_f32_e32 v162, v22
	v_exp_f32_e32 v101, v6
	v_exp_f32_e32 v164, v23
	v_exp_f32_e32 v102, v7
	v_exp_f32_e32 v150, v24
	v_exp_f32_e32 v143, v8
	v_exp_f32_e32 v154, v25
	v_exp_f32_e32 v146, v9
	v_exp_f32_e32 v152, v26
	v_exp_f32_e32 v145, v10
	v_exp_f32_e32 v157, v27
	v_exp_f32_e32 v147, v11
	v_exp_f32_e32 v149, v28
	v_exp_f32_e32 v69, v12
	v_exp_f32_e32 v153, v29
	v_exp_f32_e32 v109, v13
	v_exp_f32_e32 v151, v30
	v_exp_f32_e32 v108, v14
	v_exp_f32_e32 v156, v31
	v_exp_f32_e32 v142, v15
	v_exp_f32_e32 v155, v32
	v_exp_f32_e32 v110, v16
	v_exp_f32_e32 v159, v33
	v_exp_f32_e32 v144, v17
	v_exp_f32_e32 v158, v34
	v_exp_f32_e32 v111, v18
	v_exp_f32_e32 v160, v35
	v_exp_f32_e32 v114, v19
	v_cmp_nge_f32_e64 s[0:1], s0, v0
	v_sub_f32_e32 v0, v2, v3
	v_add_f32_e32 v36, 0xc0400000, v0
	v_mov_b32_e32 v37, v36
	v_mov_b32_e32 v38, v36
	v_mov_b32_e32 v39, v36
	v_mov_b32_e32 v40, v36
	v_mov_b32_e32 v41, v36
	v_mov_b32_e32 v42, v36
	v_mov_b32_e32 v43, v36
	v_mov_b32_e32 v44, v36
	v_mov_b32_e32 v45, v36
	v_mov_b32_e32 v46, v36
	v_mov_b32_e32 v47, v36
	v_mov_b32_e32 v48, v36
	v_mov_b32_e32 v49, v36
	v_mov_b32_e32 v50, v36
	v_mov_b32_e32 v51, v36
	v_mov_b32_e32 v4, v141
	v_mov_b32_e32 v5, v141
	v_mov_b32_e32 v6, v141
	v_mov_b32_e32 v7, v141
	v_mov_b32_e32 v8, v141
	v_mov_b32_e32 v9, v141
	v_mov_b32_e32 v10, v141
	v_mov_b32_e32 v11, v141
	v_mov_b32_e32 v12, v141
	v_mov_b32_e32 v13, v141
	v_mov_b32_e32 v14, v141
	v_mov_b32_e32 v15, v141
	v_mov_b32_e32 v16, v141
	v_mov_b32_e32 v17, v141
	v_mov_b32_e32 v18, v141
	v_mov_b32_e32 v19, v141
	v_mov_b32_e32 v20, v141
	v_mov_b32_e32 v21, v141
	v_mov_b32_e32 v22, v141
	v_mov_b32_e32 v23, v141
	v_mov_b32_e32 v24, v141
	v_mov_b32_e32 v25, v141
	v_mov_b32_e32 v26, v141
	v_mov_b32_e32 v27, v141
	v_mov_b32_e32 v28, v141
	v_mov_b32_e32 v29, v141
	v_mov_b32_e32 v30, v141
	v_mov_b32_e32 v31, v141
	v_mov_b32_e32 v32, v141
	v_mov_b32_e32 v33, v141
	v_mov_b32_e32 v34, v141
	v_mov_b32_e32 v35, v141
	v_mov_b32_e32 v0, v141
	.p2align 6
